# setprio flips removed plus one static s_setprio 1 for waves 4-7 at kernel entry
# speedup vs baseline: 1.0180x; 1.0034x over previous
; #define LAS __attribute__((address_space(3)))
; #define GAS __attribute__((address_space(1)))
; __device__ __forceinline__ unsigned xb_add(unsigned* p, unsigned v) { unsigned GAS* g = (unsigned GAS*)p; asm volatile("" : "+s"(g)); return __hip_atomic_fetch_add(g, v, __ATOMIC_RELAXED, __HIP_MEMORY_SCOPE_AGENT); }
; __device__ __forceinline__ unsigned xb_xcc_id() { return (unsigned)__builtin_amdgcn_s_getreg((3 << 11) | 20) & 0xFu; }
; __device__ __forceinline__ ArgsP args_hidden() { ArgsP p = (ArgsP)__builtin_amdgcn_kernarg_segment_ptr(); asm volatile("" : "+s"(p)); return p; }
; __device__ __forceinline__ XcdBarrier xcd_barrier_post(unsigned* bar, volatile LAS unsigned* st) {
;     XcdBarrier b; b.bar = bar; b.x = xb_xcc_id(); b.st = st;
;     if (threadIdx.x == 0) (void)xb_add(&bar[XB_XCNT(b.x)], 1u);
;     return b;
; }
; __global__ void __launch_bounds__(512, 2) fwd(Args a) {
;     ...
;     if (threadIdx.x == 0) { ((LAS unsigned*)(lds0 + LDS_BAR_OFF))[0] = 0u; ((LAS unsigned*)(lds0 + LDS_BAR_OFF))[1] = 0u; }
;     __syncthreads();
;     (void)xcd_barrier_post((unsigned*)(unsigned GAS*)(args_hidden()->ws), (volatile LAS unsigned*)(lds0 + LDS_BAR_OFF));
_ZN12_GLOBAL__N_13fwdENS_4ArgsE:
	s_mov_b64 s[86:87], s[0:1]
	v_cmp_eq_u32_e64 s[84:85], 0, v0
	v_writelane_b32 v254, s2, 0
	s_and_saveexec_b64 s[0:1], s[84:85]
	s_add_i32 s2, 0, 0x23fc0
	v_mov_b32_e32 v2, 0
	v_mov_b32_e32 v3, v2
	v_mov_b32_e32 v1, s2
	ds_write_b64 v1, v[2:3]
	s_or_b64 exec, exec, s[0:1]
	v_readfirstlane_b32 s0, v0
	s_nop 3
	s_and_b32 s0, s0, 0x3ff
	s_lshr_b32 s0, s0, 6
	s_cmp_ge_u32 s0, 4
	s_cbranch_scc0 .Lprio_done
	s_setprio 1
.Lprio_done:
	s_mov_b64 s[4:5], s[86:87]
	s_waitcnt lgkmcnt(0)
	s_barrier
	s_getreg_b32 s6, hwreg(HW_REG_XCC_ID, 0, 4)
	s_and_saveexec_b64 s[0:1], s[84:85]
	s_cbranch_execz .LBB0_5
	s_load_dwordx2 s[4:5], s[4:5], 0xa8
	s_lshl_b32 s6, s6, 8
	s_mov_b64 s[2:3], exec
	s_and_b32 s6, s6, 0xf00
	v_mbcnt_lo_u32_b32 v1, s2, 0
	s_waitcnt lgkmcnt(0)
	s_add_u32 s4, s4, s6
	s_addc_u32 s5, s5, 0
	v_mbcnt_hi_u32_b32 v1, s3, v1
	s_add_u32 s4, s4, 0x400
	v_cmp_eq_u32_e32 vcc, 0, v1
	s_addc_u32 s5, s5, 0
	s_and_b64 s[6:7], exec, vcc
	s_mov_b64 exec, s[6:7]
	s_cbranch_execz .LBB0_5
	s_bcnt1_i32_b64 s2, s[2:3]
	v_mov_b32_e32 v1, 0
	v_mov_b32_e32 v2, s2
	global_atomic_add v1, v2, s[4:5]
